# fp8 GEMM fragment ds_read_b128: odd-fq lanes read their two 16B K-halves in swapped order (A and B alike) -> conflict-free LDS reads; plus attention phase-A QK MFMAs re-interleaved into their gaps
# speedup vs baseline: 1.0455x; 1.0202x over previous
.LBB0_484:
	v_lshrrev_b32_e32 v11, 4, v9
	s_xor_b64 s[18:19], s[2:3], -1
	v_bfe_u32 v11, v11, 1, 1
	s_lshl_b32 s2, s23, 13
	v_lshl_or_b32 v15, v11, 10, s2
	s_lshl_b32 s2, s22, 5
	s_and_b32 s5, s2, 0x60
	s_lshr_b32 s2, s5, 3
	v_or_b32_e32 v11, s2, v11
	s_mov_b64 s[2:3], 0x80
	s_add_i32 m0, s49, 0x18000
	v_lshl_add_u64 v[6:7], v[6:7], 0, s[2:3]
	s_waitcnt vmcnt(2)
	s_barrier
	global_load_lds_dwordx4 v[6:7], off
	v_lshl_add_u64 v[4:5], v[4:5], 0, s[2:3]
	s_add_i32 m0, s49, 0x1a000
	s_add_i32 s65, s49, 0x8000
	global_load_lds_dwordx4 v[4:5], off
	v_lshl_add_u64 v[0:1], v[0:1], 0, s[2:3]
	s_mov_b32 m0, s65
	s_add_i32 s92, s49, 0xa000
	global_load_lds_dwordx4 v[0:1], off
	v_lshl_add_u64 v[0:1], v[2:3], 0, s[2:3]
	s_add_u32 s2, s20, 0x20080
	s_mov_b32 m0, s92
	s_addc_u32 s3, s21, 0
	global_load_lds_dwordx4 v[0:1], off
	s_add_i32 m0, s49, 0x1c000
	v_lshl_add_u64 v[0:1], s[2:3], 0, v[194:195]
	global_load_lds_dwordx4 v[0:1], off
	v_lshl_add_u64 v[0:1], s[2:3], 0, v[196:197]
	s_add_i32 m0, s49, 0x1e000
	s_cmpk_lt_u32 s9, 0x100
	global_load_lds_dwordx4 v[0:1], off
	v_mul_f32_e32 v0, 0x4f7ffffe, v8
	v_cvt_u32_f32_e32 v0, v0
	s_cselect_b64 s[20:21], -1, 0
	s_sub_i32 s2, 0, s15
	v_and_b32_e32 v10, 15, v9
	v_readfirstlane_b32 s3, v0
	v_cvt_f32_u32_e32 v0, s40
	s_mul_i32 s2, s2, s3
	s_mul_hi_u32 s2, s3, s2
	s_add_i32 s2, s3, s2
	v_rcp_iflag_f32_e32 v0, v0
	v_lshlrev_b32_e32 v13, 1, v9
	v_writelane_b32 v254, s2, 12
	s_sub_i32 s2, 0, s40
	v_mul_f32_e32 v0, 0x4f7ffffe, v0
	v_cvt_u32_f32_e32 v0, v0
	v_bfe_u32 v12, v9, 4, 2
	v_lshl_or_b32 v203, s23, 6, v10
	v_and_b32_e32 v13, 32, v13
	v_readfirstlane_b32 s3, v0
	v_lshlrev_b32_e32 v10, 6, v10
	v_lshlrev_b32_e32 v9, 2, v9
	s_mul_i32 s2, s2, s3
	v_or_b32_e32 v14, v10, v13
	v_and_b32_e32 v9, 32, v9
	v_lshlrev_b32_e32 v11, 10, v11
	s_mul_hi_u32 s2, s3, s2
	v_bitop3_b32 v10, v10, v9, v13 bitop3:0x36
	v_bitop3_b32 v205, v11, v14, v9 bitop3:0xf6
	v_or_b32_e32 v13, 16, v14
	v_bitop3_b32 v14, v14, v9, 16 bitop3:0x36
	s_waitcnt vmcnt(6)
	s_add_i32 s47, s3, s2
	v_or_b32_e32 v10, v10, v15
	v_or_b32_e32 v14, v14, v15
	s_add_u32 s46, s70, 0xee00080
	s_mov_b32 s11, s97
	v_bitop3_b32 v237, v13, v11, v9 bitop3:0xde
	v_lshl_or_b32 v238, v12, 3, s5
	s_mov_b32 s93, 0
	s_addc_u32 s9, s71, 0
	v_add_u32_e32 v239, 0, v10
	v_add_u32_e32 v240, 0, v14
	v_mbcnt_lo_u32_b32 v0, -1, 0
	v_mbcnt_hi_u32_b32 v0, -1, v0
	v_and_b32_e32 v0, 16, v0
	v_xor_b32_e32 v239, v239, v0
	v_xor_b32_e32 v240, v240, v0
	v_xor_b32_e32 v205, v205, v0
	v_xor_b32_e32 v237, v237, v0
	v_mov_b32_e32 v241, v206
	v_mov_b32_e32 v242, v96
	s_mov_b32 s51, s24
	s_barrier
	s_waitcnt vmcnt(0)
	s_branch .LBB0_487

.LBB0_726:
	v_add_u32_e32 v164, s18, v239
	ds_read_b64_tr_b16 v[190:191], v164 offset:24576
	ds_read_b64_tr_b16 v[192:193], v164 offset:25088
	s_waitcnt lgkmcnt(2)
	v_mfma_f32_32x32x16_bf16 v[48:63], v[158:161], v[110:113], v[48:63]
	v_add_f32_e32 v114, v80, v81
	v_add_f32_e32 v114, v82, v114
	v_add_f32_e32 v114, v83, v114
	v_add_f32_e32 v114, v84, v114
	v_add_f32_e32 v114, v85, v114
	v_cvt_pk_bf16_f32 v126, v80, v81
	v_cvt_pk_bf16_f32 v127, v82, v83
	ds_read_b64_tr_b16 v[186:187], v164 offset:28672
	ds_read_b64_tr_b16 v[188:189], v164 offset:29184
	v_mfma_f32_32x32x16_bf16 v[32:47], v[146:149], v[110:113], v[32:47]
	v_add_f32_e32 v80, v86, v114
	v_add_f32_e32 v80, v87, v80
	v_add_f32_e32 v80, v88, v80
	v_add_f32_e32 v80, v89, v80
	v_cvt_pk_bf16_f32 v128, v84, v85
	v_cvt_pk_bf16_f32 v129, v86, v87
	ds_read_b64_tr_b16 v[182:183], v164 offset:25600
	ds_read_b64_tr_b16 v[184:185], v164 offset:26112
	v_mfma_f32_32x32x16_bf16 v[48:63], v[154:157], v[106:109], v[48:63]
	v_add_f32_e32 v80, v90, v80
	v_add_f32_e32 v80, v91, v80
	v_add_f32_e32 v80, v92, v80
	v_add_f32_e32 v80, v93, v80
	v_cvt_pk_bf16_f32 v122, v88, v89
	v_cvt_pk_bf16_f32 v123, v90, v91
	ds_read_b64_tr_b16 v[178:179], v164 offset:29696
	ds_read_b64_tr_b16 v[180:181], v164 offset:30208
	v_mfma_f32_32x32x16_bf16 v[32:47], v[142:145], v[106:109], v[32:47]
	v_add_f32_e32 v80, v94, v80
	v_add_f32_e32 v80, v95, v80
	v_add_f32_e32 v80, v64, v80
	v_add_f32_e32 v80, v65, v80
	v_cvt_pk_bf16_f32 v124, v92, v93
	v_cvt_pk_bf16_f32 v125, v94, v95
	ds_read_b64_tr_b16 v[166:167], v164 offset:26624
	ds_read_b64_tr_b16 v[168:169], v164 offset:27136
	v_mfma_f32_32x32x16_bf16 v[48:63], v[150:153], v[102:105], v[48:63]
	v_add_f32_e32 v80, v66, v80
	v_add_f32_e32 v80, v67, v80
	v_add_f32_e32 v80, v68, v80
	v_add_f32_e32 v80, v69, v80
	v_cvt_pk_bf16_f32 v118, v64, v65
	v_cvt_pk_bf16_f32 v119, v66, v67
	ds_read_b64_tr_b16 v[174:175], v164 offset:30720
	ds_read_b64_tr_b16 v[176:177], v164 offset:31232
	v_mfma_f32_32x32x16_bf16 v[32:47], v[138:141], v[102:105], v[32:47]
	v_add_f32_e32 v64, v70, v80
	v_add_f32_e32 v64, v71, v64
	v_add_f32_e32 v64, v72, v64
	v_add_f32_e32 v64, v73, v64
	v_cvt_pk_bf16_f32 v120, v68, v69
	v_cvt_pk_bf16_f32 v121, v70, v71
	ds_read_b64_tr_b16 v[170:171], v164 offset:27648
	ds_read_b64_tr_b16 v[172:173], v164 offset:28160
	v_mfma_f32_32x32x16_bf16 v[48:63], v[134:137], v[98:101], v[48:63]
	v_add_f32_e32 v64, v74, v64
	v_add_f32_e32 v64, v75, v64
	v_add_f32_e32 v64, v76, v64
	v_add_f32_e32 v64, v77, v64
	v_cvt_pk_bf16_f32 v114, v72, v73
	v_cvt_pk_bf16_f32 v115, v74, v75
	ds_read_b64_tr_b16 v[162:163], v164 offset:31744
	ds_read_b64_tr_b16 v[164:165], v164 offset:32256
	v_mfma_f32_32x32x16_bf16 v[32:47], v[130:133], v[98:101], v[32:47]
	v_add_f32_e32 v64, v78, v64
	v_add_f32_e32 v64, v79, v64
	v_add_f32_e32 v94, 0, v64
	v_cvt_pk_bf16_f32 v116, v76, v77
	v_cvt_pk_bf16_f32 v117, v78, v79
	s_waitcnt lgkmcnt(14)
	v_lshl_add_u64 v[212:213], v[206:207], 0, s[12:13]
	s_mov_b64 s[18:19], 0x16e80000
	ds_read_b128 v[64:67], v205
	ds_read_b128 v[68:71], v205 offset:32
	ds_read_b128 v[82:85], v205 offset:128
	ds_read_b128 v[86:89], v205 offset:160
	v_lshl_add_u64 v[80:81], v[212:213], 0, s[18:19]
	s_add_i32 s18, s38, s30
	v_lshl_add_u64 v[210:211], v[208:209], 0, s[12:13]
	v_add_f32_e32 v224, v240, v94
	ds_read_b128 v[72:75], v205 offset:64
	ds_read_b128 v[76:79], v205 offset:96
	ds_read_b128 v[90:93], v205 offset:192
	ds_read_b128 v[138:141], v205 offset:224
	s_mov_b32 s19, m0
	s_mov_b32 m0, s18
	s_nop 0
	global_load_lds_dwordx4 v[80:81], off
	s_mov_b32 m0, s19
	s_mov_b64 s[18:19], 0x1ee40000
	v_lshl_add_u64 v[80:81], v[210:211], 0, s[18:19]
	s_add_i32 s18, s22, s31
	s_mov_b32 s19, m0
	s_mov_b32 m0, s18
	s_nop 0
	global_load_lds_dwordx4 v[80:81], off
	s_mov_b32 m0, s19
	v_max_f32_e32 v80, v49, v49
	v_max_f32_e32 v81, v48, v48
	v_max_f32_e32 v80, v81, v80
	v_max3_f32 v81, v50, v51, v33
	v_max3_f32 v80, v80, v32, v34
	v_max3_f32 v80, v80, v35, v52
	v_max3_f32 v81, v81, v54, v55
	v_max3_f32 v80, v80, v53, v36
	v_max3_f32 v81, v81, v38, v39
	v_max3_f32 v80, v80, v37, v56
	v_max3_f32 v81, v81, v58, v59
	v_max3_f32 v80, v80, v57, v40
	v_max3_f32 v81, v81, v42, v43
	v_max3_f32 v80, v80, v41, v60
	v_max3_f32 v81, v81, v62, v63
	v_max3_f32 v80, v80, v61, v44
	v_max3_f32 v81, v81, v46, v47
	v_max3_f32 v80, v80, v45, v81
	v_mov_b32_e32 v81, v80
	s_nop 1
	v_permlane32_swap_b32_e32 v80, v81
	v_max_f32_e32 v81, v81, v81
	v_max_f32_e32 v80, v80, v80
	v_max_f32_e32 v80, v80, v81
	v_cmp_lt_f32_e32 vcc, s51, v80
	s_cmp_lg_u64 vcc, 0
	s_cselect_b64 s[18:19], -1, 0
	s_cbranch_vccnz .LBB0_734

.LBB0_729:
	v_pk_add_f32 v[80:81], v[64:65], v[202:203] op_sel_hi:[1,0] neg_lo:[0,1] neg_hi:[0,1]
	s_waitcnt lgkmcnt(13)
	v_pk_add_f32 v[64:65], v[82:83], v[202:203] op_sel_hi:[1,0] neg_lo:[0,1] neg_hi:[0,1]
	v_pk_add_f32 v[82:83], v[66:67], v[202:203] op_sel_hi:[1,0] neg_lo:[0,1] neg_hi:[0,1]
	v_pk_add_f32 v[66:67], v[84:85], v[202:203] op_sel_hi:[1,0] neg_lo:[0,1] neg_hi:[0,1]
	v_pk_add_f32 v[84:85], v[68:69], v[202:203] op_sel_hi:[1,0] neg_lo:[0,1] neg_hi:[0,1]
	s_waitcnt lgkmcnt(12)
	v_pk_add_f32 v[68:69], v[86:87], v[202:203] op_sel_hi:[1,0] neg_lo:[0,1] neg_hi:[0,1]
	v_pk_add_f32 v[86:87], v[70:71], v[202:203] op_sel_hi:[1,0] neg_lo:[0,1] neg_hi:[0,1]
	v_pk_add_f32 v[70:71], v[88:89], v[202:203] op_sel_hi:[1,0] neg_lo:[0,1] neg_hi:[0,1]
	s_waitcnt lgkmcnt(11)
	v_pk_add_f32 v[88:89], v[72:73], v[202:203] op_sel_hi:[1,0] neg_lo:[0,1] neg_hi:[0,1]
	s_waitcnt lgkmcnt(9)
	v_pk_add_f32 v[72:73], v[90:91], v[202:203] op_sel_hi:[1,0] neg_lo:[0,1] neg_hi:[0,1]
	v_pk_add_f32 v[90:91], v[74:75], v[202:203] op_sel_hi:[1,0] neg_lo:[0,1] neg_hi:[0,1]
	v_pk_add_f32 v[74:75], v[92:93], v[202:203] op_sel_hi:[1,0] neg_lo:[0,1] neg_hi:[0,1]
	v_pk_add_f32 v[92:93], v[76:77], v[202:203] op_sel_hi:[1,0] neg_lo:[0,1] neg_hi:[0,1]
	s_waitcnt lgkmcnt(8)
	v_pk_add_f32 v[76:77], v[138:139], v[202:203] op_sel_hi:[1,0] neg_lo:[0,1] neg_hi:[0,1]
	v_pk_add_f32 v[94:95], v[78:79], v[202:203] op_sel_hi:[1,0] neg_lo:[0,1] neg_hi:[0,1]
	v_pk_add_f32 v[78:79], v[140:141], v[202:203] op_sel_hi:[1,0] neg_lo:[0,1] neg_hi:[0,1]
	s_add_i32 s18, s22, 0x2000
	v_add_u32_e32 v162, s38, v239
	ds_read_b64_tr_b16 v[194:195], v162 offset:24576
	ds_read_b64_tr_b16 v[196:197], v162 offset:25088
	s_waitcnt lgkmcnt(2)
	v_mfma_f32_32x32x16_bf16 v[80:95], v[134:137], v[110:113], v[80:95]
	v_add_f32_e32 v114, v48, v49
	v_add_f32_e32 v114, v50, v114
	v_add_f32_e32 v114, v51, v114
	v_add_f32_e32 v114, v52, v114
	v_add_f32_e32 v114, v53, v114
	v_cvt_pk_bf16_f32 v126, v48, v49
	v_cvt_pk_bf16_f32 v127, v50, v51
	ds_read_b64_tr_b16 v[190:191], v162 offset:28672
	ds_read_b64_tr_b16 v[192:193], v162 offset:29184
	v_mfma_f32_32x32x16_bf16 v[64:79], v[130:133], v[110:113], v[64:79]
	v_add_f32_e32 v48, v54, v114
	v_add_f32_e32 v48, v55, v48
	v_add_f32_e32 v48, v56, v48
	v_add_f32_e32 v48, v57, v48
	v_cvt_pk_bf16_f32 v128, v52, v53
	v_cvt_pk_bf16_f32 v129, v54, v55
	ds_read_b64_tr_b16 v[186:187], v162 offset:25600
	ds_read_b64_tr_b16 v[188:189], v162 offset:26112
	v_mfma_f32_32x32x16_bf16 v[80:95], v[146:149], v[106:109], v[80:95]
	v_add_f32_e32 v48, v58, v48
	v_add_f32_e32 v48, v59, v48
	v_add_f32_e32 v48, v60, v48
	v_add_f32_e32 v48, v61, v48
	v_cvt_pk_bf16_f32 v122, v56, v57
	v_cvt_pk_bf16_f32 v123, v58, v59
	ds_read_b64_tr_b16 v[138:139], v162 offset:29696
	ds_read_b64_tr_b16 v[140:141], v162 offset:30208
	v_mfma_f32_32x32x16_bf16 v[64:79], v[142:145], v[106:109], v[64:79]
	v_add_f32_e32 v48, v62, v48
	v_add_f32_e32 v48, v63, v48
	v_add_f32_e32 v48, v32, v48
	v_add_f32_e32 v48, v33, v48
	v_cvt_pk_bf16_f32 v124, v60, v61
	v_cvt_pk_bf16_f32 v125, v62, v63
	ds_read_b64_tr_b16 v[182:183], v162 offset:26624
	ds_read_b64_tr_b16 v[184:185], v162 offset:27136
	v_mfma_f32_32x32x16_bf16 v[80:95], v[158:161], v[102:105], v[80:95]
	v_add_f32_e32 v48, v34, v48
	v_add_f32_e32 v48, v35, v48
	v_add_f32_e32 v48, v36, v48
	v_add_f32_e32 v48, v37, v48
	v_cvt_pk_bf16_f32 v118, v32, v33
	v_cvt_pk_bf16_f32 v119, v34, v35
	ds_read_b64_tr_b16 v[178:179], v162 offset:30720
	ds_read_b64_tr_b16 v[180:181], v162 offset:31232
	v_mfma_f32_32x32x16_bf16 v[64:79], v[154:157], v[102:105], v[64:79]
	v_add_f32_e32 v32, v38, v48
	v_add_f32_e32 v32, v39, v32
	v_add_f32_e32 v32, v40, v32
	v_add_f32_e32 v32, v41, v32
	v_cvt_pk_bf16_f32 v120, v36, v37
	v_cvt_pk_bf16_f32 v121, v38, v39
	ds_read_b64_tr_b16 v[174:175], v162 offset:27648
	ds_read_b64_tr_b16 v[176:177], v162 offset:28160
	v_mfma_f32_32x32x16_bf16 v[80:95], v[166:169], v[98:101], v[80:95]
	v_add_f32_e32 v32, v42, v32
	v_add_f32_e32 v32, v43, v32
	v_add_f32_e32 v32, v44, v32
	v_add_f32_e32 v32, v45, v32
	v_cvt_pk_bf16_f32 v114, v40, v41
	v_cvt_pk_bf16_f32 v115, v42, v43
	ds_read_b64_tr_b16 v[170:171], v162 offset:31744
	ds_read_b64_tr_b16 v[172:173], v162 offset:32256
	v_mfma_f32_32x32x16_bf16 v[64:79], v[150:153], v[98:101], v[64:79]
	v_add_f32_e32 v32, v46, v32
	v_add_f32_e32 v32, v47, v32
	v_add_f32_e32 v62, 0, v32
	v_cvt_pk_bf16_f32 v116, v44, v45
	v_cvt_pk_bf16_f32 v117, v46, v47
	s_waitcnt lgkmcnt(14)
	s_cmpk_lg_i32 s22, 0x4000
	s_cselect_b32 s38, s18, 0
	s_mov_b64 s[18:19], 0x16ea0000
	ds_read_b128 v[32:35], v205 offset:256
	ds_read_b128 v[36:39], v205 offset:288
	ds_read_b128 v[50:53], v205 offset:384
	ds_read_b128 v[54:57], v205 offset:416
	ds_read_b128 v[40:43], v205 offset:320
	ds_read_b128 v[44:47], v205 offset:352
	ds_read_b128 v[58:61], v205 offset:448
	ds_read_b128 v[162:165], v205 offset:480
	v_lshl_add_u64 v[48:49], v[212:213], 0, s[18:19]
	s_add_i32 s18, s22, s30
	s_mov_b32 s19, m0
	s_mov_b32 m0, s18
	s_nop 0
	global_load_lds_dwordx4 v[48:49], off
	s_mov_b32 m0, s19
	s_mov_b64 s[18:19], 0x1ee60000
	v_lshl_add_u64 v[48:49], v[210:211], 0, s[18:19]
	s_add_i32 s18, s38, s31
	s_mov_b32 s19, m0
	s_mov_b32 m0, s18
	s_nop 0
	global_load_lds_dwordx4 v[48:49], off
	s_mov_b32 m0, s19
	v_add_f32_e32 v240, v224, v62
	v_max_f32_e32 v48, v81, v81
	v_max_f32_e32 v49, v80, v80
	v_max_f32_e32 v48, v49, v48
	v_max3_f32 v49, v82, v83, v65
	v_max3_f32 v48, v48, v64, v66
	v_max3_f32 v48, v48, v67, v84
	v_max3_f32 v49, v49, v86, v87
	v_max3_f32 v48, v48, v85, v68
	v_max3_f32 v49, v49, v70, v71
	v_max3_f32 v48, v48, v69, v88
	v_max3_f32 v49, v49, v90, v91
	v_max3_f32 v48, v48, v89, v72
	v_max3_f32 v49, v49, v74, v75
	v_max3_f32 v48, v48, v73, v92
	v_max3_f32 v49, v49, v94, v95
	v_max3_f32 v48, v48, v93, v76
	v_max3_f32 v49, v49, v78, v79
	v_max3_f32 v48, v48, v77, v49
	v_mov_b32_e32 v49, v48
	s_nop 1
	v_permlane32_swap_b32_e32 v48, v49
	v_max_f32_e32 v49, v49, v49
	v_max_f32_e32 v48, v48, v48
	v_max_f32_e32 v48, v48, v49
	v_cmp_lt_f32_e32 vcc, s51, v48
	s_cmp_lg_u64 vcc, 0
	s_cselect_b64 s[18:19], -1, 0
	s_cbranch_vccnz .LBB0_737

.LBB0_751:
	v_add_u32_e32 v96, s22, v239
	ds_read_b64_tr_b16 v[194:195], v96 offset:24576
	ds_read_b64_tr_b16 v[196:197], v96 offset:25088
	s_waitcnt lgkmcnt(2)
	v_mfma_f32_32x32x16_bf16 v[48:63], v[158:161], v[110:113], v[48:63]
	v_add_f32_e32 v114, v80, v81
	v_add_f32_e32 v114, v82, v114
	v_add_f32_e32 v114, v83, v114
	v_add_f32_e32 v114, v84, v114
	v_add_f32_e32 v114, v85, v114
	v_cvt_pk_bf16_f32 v126, v80, v81
	v_cvt_pk_bf16_f32 v127, v82, v83
	ds_read_b64_tr_b16 v[190:191], v96 offset:28672
	ds_read_b64_tr_b16 v[192:193], v96 offset:29184
	v_mfma_f32_32x32x16_bf16 v[32:47], v[146:149], v[110:113], v[32:47]
	v_add_f32_e32 v80, v86, v114
	v_add_f32_e32 v80, v87, v80
	v_add_f32_e32 v80, v88, v80
	v_add_f32_e32 v80, v89, v80
	v_cvt_pk_bf16_f32 v128, v84, v85
	v_cvt_pk_bf16_f32 v129, v86, v87
	ds_read_b64_tr_b16 v[186:187], v96 offset:25600
	ds_read_b64_tr_b16 v[188:189], v96 offset:26112
	v_mfma_f32_32x32x16_bf16 v[48:63], v[154:157], v[106:109], v[48:63]
	v_add_f32_e32 v80, v90, v80
	v_add_f32_e32 v80, v91, v80
	v_add_f32_e32 v80, v92, v80
	v_add_f32_e32 v80, v93, v80
	v_cvt_pk_bf16_f32 v122, v88, v89
	v_cvt_pk_bf16_f32 v123, v90, v91
	ds_read_b64_tr_b16 v[182:183], v96 offset:29696
	ds_read_b64_tr_b16 v[184:185], v96 offset:30208
	v_mfma_f32_32x32x16_bf16 v[32:47], v[142:145], v[106:109], v[32:47]
	v_add_f32_e32 v80, v94, v80
	v_add_f32_e32 v80, v95, v80
	v_add_f32_e32 v80, v64, v80
	v_add_f32_e32 v80, v65, v80
	v_cvt_pk_bf16_f32 v124, v92, v93
	v_cvt_pk_bf16_f32 v125, v94, v95
	ds_read_b64_tr_b16 v[178:179], v96 offset:26624
	ds_read_b64_tr_b16 v[180:181], v96 offset:27136
	v_mfma_f32_32x32x16_bf16 v[48:63], v[150:153], v[102:105], v[48:63]
	v_add_f32_e32 v80, v66, v80
	v_add_f32_e32 v80, v67, v80
	v_add_f32_e32 v80, v68, v80
	v_add_f32_e32 v80, v69, v80
	v_cvt_pk_bf16_f32 v118, v64, v65
	v_cvt_pk_bf16_f32 v119, v66, v67
	ds_read_b64_tr_b16 v[174:175], v96 offset:30720
	ds_read_b64_tr_b16 v[176:177], v96 offset:31232
	v_mfma_f32_32x32x16_bf16 v[32:47], v[138:141], v[102:105], v[32:47]
	v_add_f32_e32 v64, v70, v80
	v_add_f32_e32 v64, v71, v64
	v_add_f32_e32 v64, v72, v64
	v_add_f32_e32 v64, v73, v64
	v_cvt_pk_bf16_f32 v120, v68, v69
	v_cvt_pk_bf16_f32 v121, v70, v71
	ds_read_b64_tr_b16 v[170:171], v96 offset:27648
	ds_read_b64_tr_b16 v[172:173], v96 offset:28160
	v_mfma_f32_32x32x16_bf16 v[48:63], v[134:137], v[98:101], v[48:63]
	v_add_f32_e32 v64, v74, v64
	v_add_f32_e32 v64, v75, v64
	v_add_f32_e32 v64, v76, v64
	v_add_f32_e32 v64, v77, v64
	v_cvt_pk_bf16_f32 v114, v72, v73
	v_cvt_pk_bf16_f32 v115, v74, v75
	ds_read_b64_tr_b16 v[166:167], v96 offset:31744
	ds_read_b64_tr_b16 v[168:169], v96 offset:32256
	v_mfma_f32_32x32x16_bf16 v[32:47], v[130:133], v[98:101], v[32:47]
	v_add_f32_e32 v64, v78, v64
	v_add_f32_e32 v64, v79, v64
	v_add_f32_e32 v80, 0, v64
	v_cvt_pk_bf16_f32 v116, v76, v77
	v_cvt_pk_bf16_f32 v117, v78, v79
	s_waitcnt lgkmcnt(14)
	ds_read_b128 v[64:67], v213
	ds_read_b128 v[68:71], v213 offset:32
	ds_read_b128 v[82:85], v213 offset:128
	ds_read_b128 v[86:89], v213 offset:160
	ds_read_b128 v[72:75], v213 offset:64
	ds_read_b128 v[76:79], v213 offset:96
	ds_read_b128 v[90:93], v213 offset:192
	ds_read_b128 v[162:165], v213 offset:224
	s_add_i32 s22, s40, -1
	s_cmp_ge_u32 s22, s39
	s_cselect_b64 s[14:15], -1, 0
	s_and_b64 vcc, exec, s[14:15]
	v_lshl_add_u64 v[210:211], v[206:207], 0, s[12:13]
	s_cbranch_vccnz .LBB0_753
	s_mov_b64 s[4:5], 0x16e60000
	s_add_i32 s16, s38, s30
	v_lshl_add_u64 v[94:95], v[210:211], 0, s[4:5]
	s_mov_b32 s4, m0
	s_mov_b32 m0, s16
	s_nop 0
	global_load_lds_dwordx4 v[94:95], off
	s_mov_b32 m0, s4

.LBB0_969:
	s_add_u32 s31, s60, 0x2000
	v_readlane_b32 s2, v254, 16
	v_and_b32_e32 v9, 15, v8
	v_lshrrev_b32_e32 v10, 4, v8
	s_addc_u32 s38, s2, 0
	v_lshl_or_b32 v203, s8, 6, v9
	v_bfe_u32 v10, v10, 1, 1
	s_lshl_b32 s8, s8, 13
	s_lshl_b32 s7, s7, 5
	s_mov_b64 s[2:3], 0x80
	v_lshl_or_b32 v14, v10, 10, s8
	s_and_b32 s8, s7, 0x60
	s_add_i32 m0, s21, 0x18000
	v_lshl_add_u64 v[6:7], v[6:7], 0, s[2:3]
	s_lshr_b32 s7, s8, 3
	s_waitcnt vmcnt(2)
	s_barrier
	global_load_lds_dwordx4 v[6:7], off
	v_lshl_add_u64 v[4:5], v[4:5], 0, s[2:3]
	s_add_i32 m0, s21, 0x1a000
	s_add_i32 s39, s21, 0x8000
	s_add_i32 s40, s21, 0xa000
	global_load_lds_dwordx4 v[4:5], off
	v_lshl_add_u64 v[0:1], v[0:1], 0, s[2:3]
	s_mov_b32 m0, s39
	s_add_u32 s0, s0, 0x20080
	global_load_lds_dwordx4 v[0:1], off
	v_lshl_add_u64 v[0:1], v[2:3], 0, s[2:3]
	s_mov_b32 m0, s40
	s_addc_u32 s1, s1, 0
	global_load_lds_dwordx4 v[0:1], off
	s_add_i32 m0, s21, 0x1c000
	v_lshl_add_u64 v[0:1], s[0:1], 0, v[194:195]
	global_load_lds_dwordx4 v[0:1], off
	v_lshl_add_u64 v[0:1], s[0:1], 0, v[196:197]
	s_add_i32 m0, s21, 0x1e000
	v_lshlrev_b32_e32 v12, 1, v8
	global_load_lds_dwordx4 v[0:1], off
	v_bfe_u32 v11, v8, 4, 2
	v_and_b32_e32 v12, 32, v12
	v_lshlrev_b32_e32 v9, 6, v9
	v_lshlrev_b32_e32 v8, 2, v8
	v_or_b32_e32 v10, s7, v10
	v_or_b32_e32 v13, v9, v12
	v_and_b32_e32 v8, 32, v8
	v_lshlrev_b32_e32 v10, 10, v10
	v_bitop3_b32 v9, v9, v8, v12 bitop3:0x36
	v_bitop3_b32 v205, v10, v13, v8 bitop3:0xf6
	v_or_b32_e32 v12, 16, v13
	v_bitop3_b32 v13, v13, v8, 16 bitop3:0x36
	s_waitcnt vmcnt(6)
	s_cmpk_lt_u32 s6, 0x100
	v_or_b32_e32 v9, v9, v14
	v_or_b32_e32 v13, v13, v14
	s_cselect_b64 s[58:59], -1, 0
	s_add_u32 s41, s70, 0xee00080
	v_readlane_b32 s0, v255, 2
	v_bitop3_b32 v237, v12, v10, v8 bitop3:0xde
	v_lshl_or_b32 v238, v11, 3, s8
	s_addc_u32 s45, s71, 0
	s_mov_b32 s14, 0
	v_add_u32_e32 v239, 0, v9
	v_add_u32_e32 v240, 0, v13
	v_mbcnt_lo_u32_b32 v0, -1, 0
	v_mbcnt_hi_u32_b32 v0, -1, v0
	v_and_b32_e32 v0, 16, v0
	v_xor_b32_e32 v239, v239, v0
	v_xor_b32_e32 v240, v240, v0
	v_xor_b32_e32 v205, v205, v0
	v_xor_b32_e32 v237, v237, v0
	s_mov_b32 s23, s0
	v_readlane_b32 s22, v255, 0
	v_mov_b32_e32 v241, v206
	v_mov_b32_e32 v242, v96
	s_barrier
	v_readlane_b32 s1, v255, 3
	s_branch .LBB0_972

.LBB0_1253:
	v_and_b32_e32 v9, 15, v8
	v_lshrrev_b32_e32 v10, 4, v8
	s_lshl_b32 s2, s2, 5
	s_mov_b64 s[10:11], 0x80
	v_lshl_or_b32 v207, s3, 6, v9
	v_bfe_u32 v10, v10, 1, 1
	s_lshl_b32 s3, s3, 13
	s_and_b32 s2, s2, 0x60
	s_add_i32 m0, s40, 0x18000
	v_lshl_add_u64 v[6:7], v[6:7], 0, s[10:11]
	v_lshl_or_b32 v15, v10, 10, s3
	s_lshr_b32 s3, s2, 3
	s_waitcnt vmcnt(2)
	s_barrier
	global_load_lds_dwordx4 v[6:7], off
	v_lshl_add_u64 v[4:5], v[4:5], 0, s[10:11]
	s_add_i32 m0, s40, 0x1a000
	s_add_i32 s60, s40, 0x8000
	s_add_i32 s61, s40, 0xa000
	global_load_lds_dwordx4 v[4:5], off
	v_lshl_add_u64 v[0:1], v[0:1], 0, s[10:11]
	s_mov_b32 m0, s60
	s_add_u32 s0, s0, 0x20080
	global_load_lds_dwordx4 v[0:1], off
	v_lshl_add_u64 v[0:1], v[2:3], 0, s[10:11]
	s_mov_b32 m0, s61
	s_addc_u32 s1, s1, 0
	global_load_lds_dwordx4 v[0:1], off
	s_add_i32 m0, s40, 0x1c000
	v_lshl_add_u64 v[0:1], s[0:1], 0, v[196:197]
	global_load_lds_dwordx4 v[0:1], off
	v_lshl_add_u64 v[0:1], s[0:1], 0, v[202:203]
	s_add_i32 m0, s40, 0x1e000
	v_lshlrev_b32_e32 v12, 1, v8
	global_load_lds_dwordx4 v[0:1], off
	v_bfe_u32 v11, v8, 4, 2
	v_and_b32_e32 v12, 32, v12
	v_lshlrev_b32_e32 v13, 6, v9
	v_lshlrev_b32_e32 v8, 2, v8
	v_or_b32_e32 v10, s3, v10
	v_or_b32_e32 v14, v13, v12
	v_and_b32_e32 v8, 32, v8
	v_lshlrev_b32_e32 v10, 10, v10
	v_bitop3_b32 v12, v13, v8, v12 bitop3:0x36
	v_bitop3_b32 v209, v10, v14, v8 bitop3:0xf6
	v_or_b32_e32 v13, 16, v14
	v_bitop3_b32 v14, v14, v8, 16 bitop3:0x36
	s_waitcnt vmcnt(6)
	s_cmpk_lt_u32 s8, 0x100
	v_or_b32_e32 v12, v12, v15
	v_or_b32_e32 v14, v14, v15
	s_cselect_b64 s[8:9], -1, 0
	v_or_b32_e32 v0, v11, v9
	s_add_u32 s65, s70, 0xee00080
	v_bitop3_b32 v239, v13, v10, v8 bitop3:0xde
	s_mov_b32 s64, 0
	v_cmp_eq_u32_e64 s[0:1], 0, v0
	v_or_b32_e32 v240, 16, v207
	v_or_b32_e32 v241, 32, v207
	v_or_b32_e32 v242, 48, v207
	v_lshl_or_b32 v243, v11, 3, s2
	s_addc_u32 s80, s71, 0
	s_mov_b32 s27, -1
	v_add_u32_e32 v244, 0, v12
	v_add_u32_e32 v245, 0, v14
	v_mbcnt_lo_u32_b32 v0, -1, 0
	v_mbcnt_hi_u32_b32 v0, -1, v0
	v_and_b32_e32 v0, 16, v0
	v_xor_b32_e32 v244, v244, v0
	v_xor_b32_e32 v245, v245, v0
	v_xor_b32_e32 v209, v209, v0
	v_xor_b32_e32 v239, v239, v0
	v_mov_b32_e32 v246, v204
	v_mov_b32_e32 v247, v96
	s_barrier

.LBB0_1439:
	s_mov_b64 s[16:17], 0x80
	s_add_i32 m0, s11, 0x18000
	v_lshl_add_u64 v[6:7], v[6:7], 0, s[16:17]
	v_and_b32_e32 v9, 15, v8
	v_lshrrev_b32_e32 v10, 4, v8
	s_lshl_b32 s13, s13, 5
	s_waitcnt vmcnt(2)
	s_barrier
	global_load_lds_dwordx4 v[6:7], off
	v_lshl_add_u64 v[2:3], v[2:3], 0, s[16:17]
	s_add_i32 m0, s11, 0x1a000
	s_add_i32 s81, s11, 0x8000
	v_lshl_or_b32 v195, s15, 6, v9
	v_bfe_u32 v10, v10, 1, 1
	s_lshl_b32 s15, s15, 13
	s_and_b32 s13, s13, 0x60
	global_load_lds_dwordx4 v[2:3], off
	v_lshl_add_u64 v[0:1], v[0:1], 0, s[16:17]
	s_mov_b32 m0, s81
	v_lshl_or_b32 v14, v10, 10, s15
	s_lshr_b32 s15, s13, 3
	global_load_lds_dwordx4 v[0:1], off
	v_lshl_add_u64 v[0:1], v[4:5], 0, s[16:17]
	s_add_i32 s16, s11, 0xa000
	s_add_u32 s18, s18, 0x10080
	s_mov_b32 m0, s16
	s_addc_u32 s19, s19, 0
	global_load_lds_dwordx4 v[0:1], off
	s_add_i32 m0, s11, 0x1c000
	v_lshl_add_u64 v[0:1], s[18:19], 0, v[204:205]
	global_load_lds_dwordx4 v[0:1], off
	v_lshl_add_u64 v[0:1], s[18:19], 0, v[206:207]
	s_add_i32 m0, s11, 0x1e000
	v_bfe_u32 v11, v8, 4, 2
	global_load_lds_dwordx4 v[0:1], off
	s_cmpk_lt_u32 s12, 0x100
	v_or_b32_e32 v10, s15, v10
	s_cselect_b64 s[18:19], -1, 0
	v_lshl_or_b32 v247, v11, 3, s13
	s_abs_i32 s13, s6
	v_readlane_b32 s15, v255, 6
	s_mul_hi_u32 s15, s13, s15
	v_readlane_b32 s21, v255, 7
	s_mul_i32 s17, s15, s21
	v_readlane_b32 s12, v254, 38
	s_sub_i32 s13, s13, s17
	s_xor_b32 s12, s7, s12
	s_add_i32 s17, s15, 1
	s_sub_i32 s20, s13, s21
	s_cmp_ge_u32 s13, s21
	s_cselect_b32 s15, s17, s15
	s_cselect_b32 s13, s20, s13
	s_add_i32 s17, s15, 1
	s_cmp_ge_u32 s13, s21
	s_cselect_b32 s13, s17, s15
	s_xor_b32 s13, s13, s12
	s_sub_i32 s12, s13, s12
	v_readlane_b32 s15, v254, 3
	s_mov_b32 s36, s12
	s_mul_i32 s12, s12, s15
	s_sub_i32 s12, s6, s12
	v_lshlrev_b32_e32 v12, 1, v8
	s_lshl_b32 s13, s12, 1
	v_and_b32_e32 v12, 32, v12
	v_lshlrev_b32_e32 v9, 6, v9
	v_lshlrev_b32_e32 v8, 2, v8
	s_cmp_le_i32 s13, s15
	v_or_b32_e32 v13, v9, v12
	v_and_b32_e32 v8, 32, v8
	v_lshlrev_b32_e32 v10, 10, v10
	s_cselect_b64 s[20:21], -1, 0
	v_bitop3_b32 v9, v9, v8, v12 bitop3:0x36
	v_bitop3_b32 v197, v10, v13, v8 bitop3:0xf6
	v_or_b32_e32 v12, 16, v13
	v_bitop3_b32 v13, v13, v8, 16 bitop3:0x36
	s_waitcnt vmcnt(6)
	v_writelane_b32 v254, s20, 20
	v_or_b32_e32 v9, v9, v14
	v_or_b32_e32 v13, v13, v14
	v_add_u32_e32 v243, 0xa0, v195
	v_add_u32_e32 v245, 0xb0, v195
	v_mov_b32_e32 v64, 0
	v_writelane_b32 v254, s21, 21
	v_bitop3_b32 v237, v12, v10, v8 bitop3:0xde
	v_or_b32_e32 v238, 16, v195
	v_or_b32_e32 v239, 32, v195
	v_or_b32_e32 v240, 48, v195
	v_add_u32_e32 v241, 0x80, v195
	v_add_u32_e32 v242, 0x90, v195
	v_lshlrev_b32_e32 v244, 11, v243
	v_lshlrev_b32_e32 v246, 11, v245
	s_mov_b32 s12, 0
	v_add_u32_e32 v248, 0, v9
	v_add_u32_e32 v249, 0, v13
	v_mbcnt_lo_u32_b32 v0, -1, 0
	v_mbcnt_hi_u32_b32 v0, -1, v0
	v_and_b32_e32 v0, 16, v0
	v_xor_b32_e32 v248, v248, v0
	v_xor_b32_e32 v249, v249, v0
	v_xor_b32_e32 v197, v197, v0
	v_xor_b32_e32 v237, v237, v0
	v_mov_b32_e32 v250, v202
	v_mov_b32_e32 v251, v96
	v_mov_b32_e32 v65, v64
	v_mov_b32_e32 v66, v64
	v_mov_b32_e32 v67, v64
	v_mov_b32_e32 v68, v64
	v_mov_b32_e32 v69, v64
	v_mov_b32_e32 v70, v64
	v_mov_b32_e32 v71, v64
	v_mov_b32_e32 v72, v64
	v_mov_b32_e32 v73, v64
	v_mov_b32_e32 v74, v64
	v_mov_b32_e32 v75, v64
	v_mov_b32_e32 v76, v64
	v_mov_b32_e32 v77, v64
	v_mov_b32_e32 v78, v64
	v_mov_b32_e32 v79, v64
	v_mov_b32_e32 v80, v64
	v_mov_b32_e32 v81, v64
	v_mov_b32_e32 v82, v64
	v_mov_b32_e32 v83, v64
	v_mov_b32_e32 v84, v64
	v_mov_b32_e32 v85, v64
	v_mov_b32_e32 v86, v64
	v_mov_b32_e32 v87, v64
	v_mov_b32_e32 v88, v64
	v_mov_b32_e32 v89, v64
	v_mov_b32_e32 v90, v64
	v_mov_b32_e32 v91, v64
	v_mov_b32_e32 v92, v64
	v_mov_b32_e32 v93, v64
	v_mov_b32_e32 v94, v64
	v_mov_b32_e32 v95, v64
	v_mov_b32_e32 v98, v64
	v_mov_b32_e32 v99, v64
	v_mov_b32_e32 v100, v64
	v_mov_b32_e32 v101, v64
	v_mov_b32_e32 v102, v64
	v_mov_b32_e32 v103, v64
	v_mov_b32_e32 v104, v64
	v_mov_b32_e32 v105, v64
	v_mov_b32_e32 v106, v64
	v_mov_b32_e32 v107, v64
	v_mov_b32_e32 v108, v64
	v_mov_b32_e32 v109, v64
	v_mov_b32_e32 v110, v64
	v_mov_b32_e32 v111, v64
	v_mov_b32_e32 v112, v64
	v_mov_b32_e32 v113, v64
	v_mov_b32_e32 v114, v64
	v_mov_b32_e32 v115, v64
	v_mov_b32_e32 v116, v64
	v_mov_b32_e32 v117, v64
	v_mov_b32_e32 v118, v64
	v_mov_b32_e32 v119, v64
	v_mov_b32_e32 v120, v64
	v_mov_b32_e32 v121, v64
	v_mov_b32_e32 v122, v64
	v_mov_b32_e32 v123, v64
	v_mov_b32_e32 v124, v64
	v_mov_b32_e32 v125, v64
	v_mov_b32_e32 v126, v64
	v_mov_b32_e32 v127, v64
	v_mov_b32_e32 v128, v64
	v_mov_b32_e32 v129, v64
	v_mov_b32_e32 v130, v64
	v_mov_b32_e32 v131, v64
	v_mov_b32_e32 v132, v64
	v_mov_b32_e32 v133, v64
	v_mov_b32_e32 v134, v64
	v_mov_b32_e32 v135, v64
	v_mov_b32_e32 v136, v64
	v_mov_b32_e32 v137, v64
	v_mov_b32_e32 v138, v64
	v_mov_b32_e32 v139, v64
	v_mov_b32_e32 v140, v64
	v_mov_b32_e32 v141, v64
	v_mov_b32_e32 v142, v64
	v_mov_b32_e32 v143, v64
	v_mov_b32_e32 v144, v64
	v_mov_b32_e32 v145, v64
	v_mov_b32_e32 v146, v64
	v_mov_b32_e32 v147, v64
	v_mov_b32_e32 v148, v64
	v_mov_b32_e32 v149, v64
	v_mov_b32_e32 v150, v64
	v_mov_b32_e32 v151, v64
	v_mov_b32_e32 v152, v64
	v_mov_b32_e32 v153, v64
	v_mov_b32_e32 v158, v64
	v_mov_b32_e32 v159, v64
	v_mov_b32_e32 v160, v64
	v_mov_b32_e32 v161, v64
	v_mov_b32_e32 v162, v64
	v_mov_b32_e32 v163, v64
	v_mov_b32_e32 v164, v64
	v_mov_b32_e32 v165, v64
	v_mov_b32_e32 v154, v64
	v_mov_b32_e32 v155, v64
	v_mov_b32_e32 v156, v64
	v_mov_b32_e32 v157, v64
	v_mov_b32_e32 v166, v64
	v_mov_b32_e32 v167, v64
	v_mov_b32_e32 v168, v64
	v_mov_b32_e32 v169, v64
	v_mov_b32_e32 v170, v64
	v_mov_b32_e32 v171, v64
	v_mov_b32_e32 v172, v64
	v_mov_b32_e32 v173, v64
	v_mov_b32_e32 v174, v64
	v_mov_b32_e32 v175, v64
	v_mov_b32_e32 v176, v64
	v_mov_b32_e32 v177, v64
	v_mov_b32_e32 v178, v64
	v_mov_b32_e32 v179, v64
	v_mov_b32_e32 v180, v64
	v_mov_b32_e32 v181, v64
	v_mov_b32_e32 v182, v64
	v_mov_b32_e32 v183, v64
	v_mov_b32_e32 v184, v64
	v_mov_b32_e32 v185, v64
	v_mov_b32_e32 v186, v64
	v_mov_b32_e32 v187, v64
	v_mov_b32_e32 v188, v64
	v_mov_b32_e32 v189, v64
	v_mov_b32_e32 v190, v64
	v_mov_b32_e32 v191, v64
	v_mov_b32_e32 v192, v64
	v_mov_b32_e32 v193, v64
	v_readlane_b32 s37, v254, 16
	s_barrier
	s_branch .LBB0_1442

.LBB0_1585:
	v_and_b32_e32 v12, 15, v8
	v_lshrrev_b32_e32 v13, 4, v8
	s_lshl_b32 s19, s19, 5
	v_lshl_or_b32 v86, s20, 6, v12
	v_bfe_u32 v13, v13, 1, 1
	s_lshl_b32 s20, s20, 13
	s_and_b32 s19, s19, 0x60
	s_mov_b64 s[28:29], 0x80
	v_lshl_or_b32 v16, v13, 10, s20
	s_lshr_b32 s20, s19, 3
	s_add_i32 m0, s7, 0x18000
	v_lshl_add_u64 v[6:7], v[6:7], 0, s[28:29]
	v_or_b32_e32 v13, s20, v13
	s_waitcnt vmcnt(2)
	s_barrier
	global_load_lds_dwordx4 v[6:7], off
	v_lshl_add_u64 v[4:5], v[4:5], 0, s[28:29]
	s_add_i32 m0, s7, 0x1a000
	s_add_i32 s20, s7, 0x8000
	s_add_i32 s21, s7, 0xa000
	global_load_lds_dwordx4 v[4:5], off
	v_lshl_add_u64 v[2:3], v[2:3], 0, s[28:29]
	s_mov_b32 m0, s20
	v_lshl_add_u64 v[0:1], v[0:1], 0, s[28:29]
	s_add_u32 s28, s8, 0x10080
	global_load_lds_dwordx4 v[2:3], off
	s_mov_b32 m0, s21
	s_addc_u32 s29, s9, 0
	s_add_i32 s8, s7, 0x1c000
	global_load_lds_dwordx4 v[0:1], off
	v_lshl_add_u64 v[0:1], s[28:29], 0, v[96:97]
	s_mov_b32 m0, s8
	s_add_i32 s9, s7, 0x1e000
	global_load_lds_dwordx4 v[0:1], off
	v_lshl_add_u64 v[0:1], s[28:29], 0, v[72:73]
	s_mov_b32 m0, s9
	s_cmp_lt_u32 s22, 5
	global_load_lds_dwordx4 v[0:1], off
	s_cselect_b32 s23, 1, 2
	s_min_u32 s26, s22, 4
	s_add_i32 s25, s22, 1
	s_add_i32 s26, s26, -1
	s_cmp_lt_i32 s22, 3
	s_cselect_b32 s23, 0, s23
	s_cselect_b32 s25, s25, s26
	s_or_b32 s23, s23, s24
	s_add_i32 s24, s25, s24
	s_add_u32 s4, s59, s4
	s_addc_u32 s5, s60, s5
	s_add_u32 s25, s4, s0
	s_addc_u32 s26, s5, s1
	s_add_u32 s0, s70, 0x2ee00080
	v_lshlrev_b32_e32 v0, 13, v9
	s_addc_u32 s1, s71, 0
	s_add_i32 s4, s27, 0x30000
	v_and_b32_e32 v2, 0xffffc000, v0
	v_lshlrev_b32_e32 v3, 10, v10
	v_and_b32_e32 v1, 1, v9
	v_lshlrev_b32_e32 v14, 1, v8
	v_add3_u32 v0, s4, v2, v3
	v_lshlrev_b32_e32 v4, 6, v1
	v_lshlrev_b32_e32 v5, 1, v11
	v_bfe_u32 v79, v8, 4, 2
	v_and_b32_e32 v14, 32, v14
	v_lshlrev_b32_e32 v12, 6, v12
	v_lshlrev_b32_e32 v8, 2, v8
	v_add3_u32 v0, v0, v4, v5
	v_mov_b32_e32 v1, v97
	s_add_i32 s27, s27, 0x20000
	v_or_b32_e32 v15, v12, v14
	v_and_b32_e32 v8, 32, v8
	v_lshlrev_b32_e32 v13, 10, v13
	v_lshl_add_u64 v[74:75], s[0:1], 0, v[0:1]
	v_add3_u32 v0, s27, v2, v3
	v_bitop3_b32 v12, v12, v8, v14 bitop3:0x36
	v_bitop3_b32 v80, v13, v15, v8 bitop3:0xf6
	v_or_b32_e32 v14, 16, v15
	v_bitop3_b32 v15, v15, v8, 16 bitop3:0x36
	s_waitcnt vmcnt(6)
	v_add3_u32 v0, v0, v4, v5
	v_or_b32_e32 v12, v12, v16
	v_or_b32_e32 v15, v15, v16
	v_lshl_add_u64 v[76:77], s[0:1], 0, v[0:1]
	v_mov_b32_e32 v0, 0
	v_mov_b32_e32 v69, v97
	v_mov_b32_e32 v71, v97
	v_bitop3_b32 v81, v14, v13, v8 bitop3:0xde
	s_mov_b32 s22, 0
	s_mov_b64 s[0:1], 0
	v_add_u32_e32 v82, 0, v12
	v_add_u32_e32 v83, 0, v15
	v_mbcnt_lo_u32_b32 v84, -1, 0
	v_mbcnt_hi_u32_b32 v84, -1, v84
	v_and_b32_e32 v84, 16, v84
	v_xor_b32_e32 v82, v82, v84
	v_xor_b32_e32 v83, v83, v84
	v_xor_b32_e32 v80, v80, v84
	v_xor_b32_e32 v81, v81, v84
	v_mov_b32_e32 v1, v0
	v_mov_b32_e32 v2, v0
	v_mov_b32_e32 v3, v0
	v_mov_b32_e32 v4, v0
	v_mov_b32_e32 v5, v0
	v_mov_b32_e32 v6, v0
	v_mov_b32_e32 v7, v0
	v_mov_b32_e32 v8, v0
	v_mov_b32_e32 v9, v0
	v_mov_b32_e32 v10, v0
	v_mov_b32_e32 v11, v0
	v_mov_b32_e32 v12, v0
	v_mov_b32_e32 v13, v0
	v_mov_b32_e32 v14, v0
	v_mov_b32_e32 v15, v0
	v_mov_b32_e32 v16, v0
	v_mov_b32_e32 v17, v0
	v_mov_b32_e32 v18, v0
	v_mov_b32_e32 v19, v0
	v_mov_b32_e32 v20, v0
	v_mov_b32_e32 v21, v0
	v_mov_b32_e32 v22, v0
	v_mov_b32_e32 v23, v0
	v_mov_b32_e32 v24, v0
	v_mov_b32_e32 v25, v0
	v_mov_b32_e32 v26, v0
	v_mov_b32_e32 v27, v0
	v_mov_b32_e32 v28, v0
	v_mov_b32_e32 v29, v0
	v_mov_b32_e32 v30, v0
	v_mov_b32_e32 v31, v0
	v_mov_b32_e32 v32, v0
	v_mov_b32_e32 v33, v0
	v_mov_b32_e32 v34, v0
	v_mov_b32_e32 v35, v0
	v_mov_b32_e32 v36, v0
	v_mov_b32_e32 v37, v0
	v_mov_b32_e32 v38, v0
	v_mov_b32_e32 v39, v0
	v_mov_b32_e32 v40, v0
	v_mov_b32_e32 v41, v0
	v_mov_b32_e32 v42, v0
	v_mov_b32_e32 v43, v0
	v_mov_b32_e32 v44, v0
	v_mov_b32_e32 v45, v0
	v_mov_b32_e32 v46, v0
	v_mov_b32_e32 v47, v0
	v_mov_b32_e32 v48, v0
	v_mov_b32_e32 v49, v0
	v_mov_b32_e32 v50, v0
	v_mov_b32_e32 v51, v0
	v_mov_b32_e32 v52, v0
	v_mov_b32_e32 v53, v0
	v_mov_b32_e32 v54, v0
	v_mov_b32_e32 v55, v0
	v_mov_b32_e32 v56, v0
	v_mov_b32_e32 v57, v0
	v_mov_b32_e32 v58, v0
	v_mov_b32_e32 v59, v0
	v_mov_b32_e32 v60, v0
	v_mov_b32_e32 v61, v0
	v_mov_b32_e32 v62, v0
	v_mov_b32_e32 v63, v0
	s_barrier
